# G2 epilogue (bf16 residual path): residual tile loads software-pipelined 8 deep instead of load-wait-store per piece
# speedup vs baseline: 1.0257x; 1.0011x over previous
.Lg2epi_fast:
	s_mov_b32 s100, 0x8000
	s_mov_b32 s101, 0
	v_ashrrev_i32_e32 v167, 31, v166
	v_lshlrev_b64 v[168:169], 11, v[166:167]
	v_lshl_add_u64 v[168:169], s[18:19], 0, v[168:169]
	v_lshlrev_b32_e32 v176, 1, v64
	v_mov_b32_e32 v177, v65
	v_lshl_add_u64 v[168:169], v[168:169], 0, v[176:177]
	v_mov_b64_e32 v[188:189], v[168:169]
	v_mov_b64_e32 v[190:191], v[168:169]
	global_load_dwordx4 v[212:215], v[188:189], off
	global_load_dwordx4 v[216:219], v[188:189], off offset:256
	v_lshl_add_u64 v[188:189], v[188:189], 0, s[100:101]
	global_load_dwordx4 v[220:223], v[188:189], off
	global_load_dwordx4 v[224:227], v[188:189], off offset:256
	v_lshl_add_u64 v[188:189], v[188:189], 0, s[100:101]
	global_load_dwordx4 v[228:231], v[188:189], off
	global_load_dwordx4 v[232:235], v[188:189], off offset:256
	v_lshl_add_u64 v[188:189], v[188:189], 0, s[100:101]
	global_load_dwordx4 v[180:183], v[188:189], off
	global_load_dwordx4 v[184:187], v[188:189], off offset:256
	v_lshl_add_u64 v[188:189], s[100:101], 3, v[168:169]
	s_waitcnt vmcnt(7)
	v_lshlrev_b32_e32 v192, 16, v212
	v_and_b32_e32 v193, 0xffff0000, v212
	v_lshlrev_b32_e32 v194, 16, v213
	v_and_b32_e32 v195, 0xffff0000, v213
	v_pk_fma_f32 v[142:143], v[142:143], v[78:79], v[192:193]
	v_pk_fma_f32 v[144:145], v[144:145], v[80:81], v[194:195]
	v_lshlrev_b32_e32 v192, 16, v214
	v_and_b32_e32 v193, 0xffff0000, v214
	v_lshlrev_b32_e32 v194, 16, v215
	v_and_b32_e32 v195, 0xffff0000, v215
	v_pk_fma_f32 v[138:139], v[138:139], v[74:75], v[192:193]
	v_pk_fma_f32 v[140:141], v[140:141], v[76:77], v[194:195]
	v_cvt_pk_bf16_f32 v212, v142, v143
	v_cvt_pk_bf16_f32 v213, v144, v145
	v_cvt_pk_bf16_f32 v214, v138, v139
	v_cvt_pk_bf16_f32 v215, v140, v141
	global_store_dwordx4 v[190:191], v[212:215], off
	s_nop 1
	global_load_dwordx4 v[212:215], v[188:189], off
	s_waitcnt vmcnt(8)
	v_lshlrev_b32_e32 v192, 16, v216
	v_and_b32_e32 v193, 0xffff0000, v216
	v_lshlrev_b32_e32 v194, 16, v217
	v_and_b32_e32 v195, 0xffff0000, v217
	v_pk_fma_f32 v[134:135], v[134:135], v[70:71], v[192:193]
	v_pk_fma_f32 v[136:137], v[136:137], v[72:73], v[194:195]
	v_lshlrev_b32_e32 v192, 16, v218
	v_and_b32_e32 v193, 0xffff0000, v218
	v_lshlrev_b32_e32 v194, 16, v219
	v_and_b32_e32 v195, 0xffff0000, v219
	v_pk_fma_f32 v[130:131], v[130:131], v[66:67], v[192:193]
	v_pk_fma_f32 v[132:133], v[132:133], v[68:69], v[194:195]
	v_cvt_pk_bf16_f32 v216, v134, v135
	v_cvt_pk_bf16_f32 v217, v136, v137
	v_cvt_pk_bf16_f32 v218, v130, v131
	v_cvt_pk_bf16_f32 v219, v132, v133
	global_store_dwordx4 v[190:191], v[216:219], off offset:256
	v_lshl_add_u64 v[190:191], v[190:191], 0, s[100:101]
	global_load_dwordx4 v[216:219], v[188:189], off offset:256
	v_lshl_add_u64 v[188:189], v[188:189], 0, s[100:101]
	s_waitcnt vmcnt(9)
	v_lshlrev_b32_e32 v192, 16, v220
	v_and_b32_e32 v193, 0xffff0000, v220
	v_lshlrev_b32_e32 v194, 16, v221
	v_and_b32_e32 v195, 0xffff0000, v221
	v_pk_fma_f32 v[126:127], v[126:127], v[78:79], v[192:193]
	v_pk_fma_f32 v[128:129], v[128:129], v[80:81], v[194:195]
	v_lshlrev_b32_e32 v192, 16, v222
	v_and_b32_e32 v193, 0xffff0000, v222
	v_lshlrev_b32_e32 v194, 16, v223
	v_and_b32_e32 v195, 0xffff0000, v223
	v_pk_fma_f32 v[122:123], v[122:123], v[74:75], v[192:193]
	v_pk_fma_f32 v[124:125], v[124:125], v[76:77], v[194:195]
	v_cvt_pk_bf16_f32 v220, v126, v127
	v_cvt_pk_bf16_f32 v221, v128, v129
	v_cvt_pk_bf16_f32 v222, v122, v123
	v_cvt_pk_bf16_f32 v223, v124, v125
	global_store_dwordx4 v[190:191], v[220:223], off
	s_nop 1
	global_load_dwordx4 v[220:223], v[188:189], off
	s_waitcnt vmcnt(10)
	v_lshlrev_b32_e32 v192, 16, v224
	v_and_b32_e32 v193, 0xffff0000, v224
	v_lshlrev_b32_e32 v194, 16, v225
	v_and_b32_e32 v195, 0xffff0000, v225
	v_pk_fma_f32 v[118:119], v[118:119], v[70:71], v[192:193]
	v_pk_fma_f32 v[120:121], v[120:121], v[72:73], v[194:195]
	v_lshlrev_b32_e32 v192, 16, v226
	v_and_b32_e32 v193, 0xffff0000, v226
	v_lshlrev_b32_e32 v194, 16, v227
	v_and_b32_e32 v195, 0xffff0000, v227
	v_pk_fma_f32 v[114:115], v[114:115], v[66:67], v[192:193]
	v_pk_fma_f32 v[116:117], v[116:117], v[68:69], v[194:195]
	v_cvt_pk_bf16_f32 v224, v118, v119
	v_cvt_pk_bf16_f32 v225, v120, v121
	v_cvt_pk_bf16_f32 v226, v114, v115
	v_cvt_pk_bf16_f32 v227, v116, v117
	global_store_dwordx4 v[190:191], v[224:227], off offset:256
	v_lshl_add_u64 v[190:191], v[190:191], 0, s[100:101]
	global_load_dwordx4 v[224:227], v[188:189], off offset:256
	v_lshl_add_u64 v[188:189], v[188:189], 0, s[100:101]
	s_waitcnt vmcnt(11)
	v_lshlrev_b32_e32 v192, 16, v228
	v_and_b32_e32 v193, 0xffff0000, v228
	v_lshlrev_b32_e32 v194, 16, v229
	v_and_b32_e32 v195, 0xffff0000, v229
	v_pk_fma_f32 v[110:111], v[110:111], v[78:79], v[192:193]
	v_pk_fma_f32 v[112:113], v[112:113], v[80:81], v[194:195]
	v_lshlrev_b32_e32 v192, 16, v230
	v_and_b32_e32 v193, 0xffff0000, v230
	v_lshlrev_b32_e32 v194, 16, v231
	v_and_b32_e32 v195, 0xffff0000, v231
	v_pk_fma_f32 v[106:107], v[106:107], v[74:75], v[192:193]
	v_pk_fma_f32 v[108:109], v[108:109], v[76:77], v[194:195]
	v_cvt_pk_bf16_f32 v228, v110, v111
	v_cvt_pk_bf16_f32 v229, v112, v113
	v_cvt_pk_bf16_f32 v230, v106, v107
	v_cvt_pk_bf16_f32 v231, v108, v109
	global_store_dwordx4 v[190:191], v[228:231], off
	s_nop 1
	global_load_dwordx4 v[228:231], v[188:189], off
	s_waitcnt vmcnt(12)
	v_lshlrev_b32_e32 v192, 16, v232
	v_and_b32_e32 v193, 0xffff0000, v232
	v_lshlrev_b32_e32 v194, 16, v233
	v_and_b32_e32 v195, 0xffff0000, v233
	v_pk_fma_f32 v[102:103], v[102:103], v[70:71], v[192:193]
	v_pk_fma_f32 v[104:105], v[104:105], v[72:73], v[194:195]
	v_lshlrev_b32_e32 v192, 16, v234
	v_and_b32_e32 v193, 0xffff0000, v234
	v_lshlrev_b32_e32 v194, 16, v235
	v_and_b32_e32 v195, 0xffff0000, v235
	v_pk_fma_f32 v[98:99], v[98:99], v[66:67], v[192:193]
	v_pk_fma_f32 v[100:101], v[100:101], v[68:69], v[194:195]
	v_cvt_pk_bf16_f32 v232, v102, v103
	v_cvt_pk_bf16_f32 v233, v104, v105
	v_cvt_pk_bf16_f32 v234, v98, v99
	v_cvt_pk_bf16_f32 v235, v100, v101
	global_store_dwordx4 v[190:191], v[232:235], off offset:256
	v_lshl_add_u64 v[190:191], v[190:191], 0, s[100:101]
	global_load_dwordx4 v[232:235], v[188:189], off offset:256
	v_lshl_add_u64 v[188:189], v[188:189], 0, s[100:101]
	s_waitcnt vmcnt(13)
	v_lshlrev_b32_e32 v192, 16, v180
	v_and_b32_e32 v193, 0xffff0000, v180
	v_lshlrev_b32_e32 v194, 16, v181
	v_and_b32_e32 v195, 0xffff0000, v181
	v_pk_fma_f32 v[94:95], v[94:95], v[78:79], v[192:193]
	v_pk_fma_f32 v[96:97], v[96:97], v[80:81], v[194:195]
	v_lshlrev_b32_e32 v192, 16, v182
	v_and_b32_e32 v193, 0xffff0000, v182
	v_lshlrev_b32_e32 v194, 16, v183
	v_and_b32_e32 v195, 0xffff0000, v183
	v_pk_fma_f32 v[90:91], v[90:91], v[74:75], v[192:193]
	v_pk_fma_f32 v[92:93], v[92:93], v[76:77], v[194:195]
	v_cvt_pk_bf16_f32 v180, v94, v95
	v_cvt_pk_bf16_f32 v181, v96, v97
	v_cvt_pk_bf16_f32 v182, v90, v91
	v_cvt_pk_bf16_f32 v183, v92, v93
	global_store_dwordx4 v[190:191], v[180:183], off
	s_nop 1
	global_load_dwordx4 v[180:183], v[188:189], off
	s_waitcnt vmcnt(14)
	v_lshlrev_b32_e32 v192, 16, v184
	v_and_b32_e32 v193, 0xffff0000, v184
	v_lshlrev_b32_e32 v194, 16, v185
	v_and_b32_e32 v195, 0xffff0000, v185
	v_pk_fma_f32 v[86:87], v[86:87], v[70:71], v[192:193]
	v_pk_fma_f32 v[88:89], v[88:89], v[72:73], v[194:195]
	v_lshlrev_b32_e32 v192, 16, v186
	v_and_b32_e32 v193, 0xffff0000, v186
	v_lshlrev_b32_e32 v194, 16, v187
	v_and_b32_e32 v195, 0xffff0000, v187
	v_pk_fma_f32 v[82:83], v[82:83], v[66:67], v[192:193]
	v_pk_fma_f32 v[84:85], v[84:85], v[68:69], v[194:195]
	v_cvt_pk_bf16_f32 v184, v86, v87
	v_cvt_pk_bf16_f32 v185, v88, v89
	v_cvt_pk_bf16_f32 v186, v82, v83
	v_cvt_pk_bf16_f32 v187, v84, v85
	global_store_dwordx4 v[190:191], v[184:187], off offset:256
	v_lshl_add_u64 v[190:191], s[100:101], 3, v[168:169]
	global_load_dwordx4 v[184:187], v[188:189], off offset:256
	s_waitcnt vmcnt(14)
	v_lshlrev_b32_e32 v192, 16, v212
	v_and_b32_e32 v193, 0xffff0000, v212
	v_lshlrev_b32_e32 v194, 16, v213
	v_and_b32_e32 v195, 0xffff0000, v213
	v_pk_fma_f32 v[60:61], v[60:61], v[78:79], v[192:193]
	v_pk_fma_f32 v[62:63], v[62:63], v[80:81], v[194:195]
	v_lshlrev_b32_e32 v192, 16, v214
	v_and_b32_e32 v193, 0xffff0000, v214
	v_lshlrev_b32_e32 v194, 16, v215
	v_and_b32_e32 v195, 0xffff0000, v215
	v_pk_fma_f32 v[56:57], v[56:57], v[74:75], v[192:193]
	v_pk_fma_f32 v[58:59], v[58:59], v[76:77], v[194:195]
	v_cvt_pk_bf16_f32 v212, v60, v61
	v_cvt_pk_bf16_f32 v213, v62, v63
	v_cvt_pk_bf16_f32 v214, v56, v57
	v_cvt_pk_bf16_f32 v215, v58, v59
	global_store_dwordx4 v[190:191], v[212:215], off
	s_nop 1
	s_waitcnt vmcnt(13)
	v_lshlrev_b32_e32 v192, 16, v216
	v_and_b32_e32 v193, 0xffff0000, v216
	v_lshlrev_b32_e32 v194, 16, v217
	v_and_b32_e32 v195, 0xffff0000, v217
	v_pk_fma_f32 v[52:53], v[52:53], v[70:71], v[192:193]
	v_pk_fma_f32 v[54:55], v[54:55], v[72:73], v[194:195]
	v_lshlrev_b32_e32 v192, 16, v218
	v_and_b32_e32 v193, 0xffff0000, v218
	v_lshlrev_b32_e32 v194, 16, v219
	v_and_b32_e32 v195, 0xffff0000, v219
	v_pk_fma_f32 v[48:49], v[48:49], v[66:67], v[192:193]
	v_pk_fma_f32 v[50:51], v[50:51], v[68:69], v[194:195]
	v_cvt_pk_bf16_f32 v216, v52, v53
	v_cvt_pk_bf16_f32 v217, v54, v55
	v_cvt_pk_bf16_f32 v218, v48, v49
	v_cvt_pk_bf16_f32 v219, v50, v51
	global_store_dwordx4 v[190:191], v[216:219], off offset:256
	v_lshl_add_u64 v[190:191], v[190:191], 0, s[100:101]
	s_waitcnt vmcnt(12)
	v_lshlrev_b32_e32 v192, 16, v220
	v_and_b32_e32 v193, 0xffff0000, v220
	v_lshlrev_b32_e32 v194, 16, v221
	v_and_b32_e32 v195, 0xffff0000, v221
	v_pk_fma_f32 v[44:45], v[44:45], v[78:79], v[192:193]
	v_pk_fma_f32 v[46:47], v[46:47], v[80:81], v[194:195]
	v_lshlrev_b32_e32 v192, 16, v222
	v_and_b32_e32 v193, 0xffff0000, v222
	v_lshlrev_b32_e32 v194, 16, v223
	v_and_b32_e32 v195, 0xffff0000, v223
	v_pk_fma_f32 v[40:41], v[40:41], v[74:75], v[192:193]
	v_pk_fma_f32 v[42:43], v[42:43], v[76:77], v[194:195]
	v_cvt_pk_bf16_f32 v220, v44, v45
	v_cvt_pk_bf16_f32 v221, v46, v47
	v_cvt_pk_bf16_f32 v222, v40, v41
	v_cvt_pk_bf16_f32 v223, v42, v43
	global_store_dwordx4 v[190:191], v[220:223], off
	s_nop 1
	s_waitcnt vmcnt(11)
	v_lshlrev_b32_e32 v192, 16, v224
	v_and_b32_e32 v193, 0xffff0000, v224
	v_lshlrev_b32_e32 v194, 16, v225
	v_and_b32_e32 v195, 0xffff0000, v225
	v_pk_fma_f32 v[36:37], v[36:37], v[70:71], v[192:193]
	v_pk_fma_f32 v[38:39], v[38:39], v[72:73], v[194:195]
	v_lshlrev_b32_e32 v192, 16, v226
	v_and_b32_e32 v193, 0xffff0000, v226
	v_lshlrev_b32_e32 v194, 16, v227
	v_and_b32_e32 v195, 0xffff0000, v227
	v_pk_fma_f32 v[32:33], v[32:33], v[66:67], v[192:193]
	v_pk_fma_f32 v[34:35], v[34:35], v[68:69], v[194:195]
	v_cvt_pk_bf16_f32 v224, v36, v37
	v_cvt_pk_bf16_f32 v225, v38, v39
	v_cvt_pk_bf16_f32 v226, v32, v33
	v_cvt_pk_bf16_f32 v227, v34, v35
	global_store_dwordx4 v[190:191], v[224:227], off offset:256
	v_lshl_add_u64 v[190:191], v[190:191], 0, s[100:101]
	s_waitcnt vmcnt(10)
	v_lshlrev_b32_e32 v192, 16, v228
	v_and_b32_e32 v193, 0xffff0000, v228
	v_lshlrev_b32_e32 v194, 16, v229
	v_and_b32_e32 v195, 0xffff0000, v229
	v_pk_fma_f32 v[28:29], v[28:29], v[78:79], v[192:193]
	v_pk_fma_f32 v[30:31], v[30:31], v[80:81], v[194:195]
	v_lshlrev_b32_e32 v192, 16, v230
	v_and_b32_e32 v193, 0xffff0000, v230
	v_lshlrev_b32_e32 v194, 16, v231
	v_and_b32_e32 v195, 0xffff0000, v231
	v_pk_fma_f32 v[24:25], v[24:25], v[74:75], v[192:193]
	v_pk_fma_f32 v[26:27], v[26:27], v[76:77], v[194:195]
	v_cvt_pk_bf16_f32 v228, v28, v29
	v_cvt_pk_bf16_f32 v229, v30, v31
	v_cvt_pk_bf16_f32 v230, v24, v25
	v_cvt_pk_bf16_f32 v231, v26, v27
	global_store_dwordx4 v[190:191], v[228:231], off
	s_nop 1
	s_waitcnt vmcnt(9)
	v_lshlrev_b32_e32 v192, 16, v232
	v_and_b32_e32 v193, 0xffff0000, v232
	v_lshlrev_b32_e32 v194, 16, v233
	v_and_b32_e32 v195, 0xffff0000, v233
	v_pk_fma_f32 v[20:21], v[20:21], v[70:71], v[192:193]
	v_pk_fma_f32 v[22:23], v[22:23], v[72:73], v[194:195]
	v_lshlrev_b32_e32 v192, 16, v234
	v_and_b32_e32 v193, 0xffff0000, v234
	v_lshlrev_b32_e32 v194, 16, v235
	v_and_b32_e32 v195, 0xffff0000, v235
	v_pk_fma_f32 v[16:17], v[16:17], v[66:67], v[192:193]
	v_pk_fma_f32 v[18:19], v[18:19], v[68:69], v[194:195]
	v_cvt_pk_bf16_f32 v232, v20, v21
	v_cvt_pk_bf16_f32 v233, v22, v23
	v_cvt_pk_bf16_f32 v234, v16, v17
	v_cvt_pk_bf16_f32 v235, v18, v19
	global_store_dwordx4 v[190:191], v[232:235], off offset:256
	v_lshl_add_u64 v[190:191], v[190:191], 0, s[100:101]
	s_waitcnt vmcnt(8)
	v_lshlrev_b32_e32 v192, 16, v180
	v_and_b32_e32 v193, 0xffff0000, v180
	v_lshlrev_b32_e32 v194, 16, v181
	v_and_b32_e32 v195, 0xffff0000, v181
	v_pk_fma_f32 v[12:13], v[12:13], v[78:79], v[192:193]
	v_pk_fma_f32 v[14:15], v[14:15], v[80:81], v[194:195]
	v_lshlrev_b32_e32 v192, 16, v182
	v_and_b32_e32 v193, 0xffff0000, v182
	v_lshlrev_b32_e32 v194, 16, v183
	v_and_b32_e32 v195, 0xffff0000, v183
	v_pk_fma_f32 v[8:9], v[8:9], v[74:75], v[192:193]
	v_pk_fma_f32 v[10:11], v[10:11], v[76:77], v[194:195]
	v_cvt_pk_bf16_f32 v180, v12, v13
	v_cvt_pk_bf16_f32 v181, v14, v15
	v_cvt_pk_bf16_f32 v182, v8, v9
	v_cvt_pk_bf16_f32 v183, v10, v11
	global_store_dwordx4 v[190:191], v[180:183], off
	s_nop 1
	s_waitcnt vmcnt(7)
	v_lshlrev_b32_e32 v192, 16, v184
	v_and_b32_e32 v193, 0xffff0000, v184
	v_lshlrev_b32_e32 v194, 16, v185
	v_and_b32_e32 v195, 0xffff0000, v185
	v_pk_fma_f32 v[4:5], v[4:5], v[70:71], v[192:193]
	v_pk_fma_f32 v[6:7], v[6:7], v[72:73], v[194:195]
	v_lshlrev_b32_e32 v192, 16, v186
	v_and_b32_e32 v193, 0xffff0000, v186
	v_lshlrev_b32_e32 v194, 16, v187
	v_and_b32_e32 v195, 0xffff0000, v187
	v_pk_fma_f32 v[0:1], v[0:1], v[66:67], v[192:193]
	v_pk_fma_f32 v[2:3], v[2:3], v[68:69], v[194:195]
	v_cvt_pk_bf16_f32 v184, v4, v5
	v_cvt_pk_bf16_f32 v185, v6, v7
	v_cvt_pk_bf16_f32 v186, v0, v1
	v_cvt_pk_bf16_f32 v187, v2, v3
	global_store_dwordx4 v[190:191], v[184:187], off offset:256
	s_andn2_b64 vcc, exec, s[24:25]
	s_mov_b64 s[0:1], -1
	s_branch .Lg2epi_join

.Lg2epi_join:
	s_cbranch_vccnz .LBB0_812
	s_andn2_b64 vcc, exec, s[16:17]
	s_cbranch_vccnz .LBB0_811
	s_barrier
	s_branch .LBB0_811
